# baseline (speedup 1.0000x reference)
.Lfp_partend:
	ds_write_b128 v136, v[66:69]
	ds_write_b128 v136, v[70:73] offset:64
	ds_write_b128 v136, v[74:77] offset:128
	ds_write_b128 v136, v[78:81] offset:192
	s_cmp_eq_u32 s66, 0
	s_cbranch_scc0 .Lfp_pe1
	ds_read_b128 v[126:129], v137
	ds_read_b128 v[114:117], v138
	ds_read_b128 v[118:121], v138 offset:1024
	ds_read_b128 v[122:125], v138 offset:2048
	ds_read_b128 v[66:69], v138 offset:3072
	ds_read_b128 v[70:73], v138 offset:4096
	ds_read_b128 v[74:77], v138 offset:5120
	ds_read_b128 v[78:81], v138 offset:6144
	s_waitcnt lgkmcnt(6)
	v_mfma_f32_16x16x32_f16 v[82:85], v[126:129], v[114:117], v[82:85]
	ds_read_b128 v[114:117], v138 offset:7168
	s_waitcnt lgkmcnt(6)
	v_mfma_f32_16x16x32_f16 v[86:89], v[126:129], v[118:121], v[86:89]
	ds_read_b128 v[130:133], v137 offset:64
	ds_read_b128 v[118:121], v138 offset:8192
	s_waitcnt lgkmcnt(7)
	v_mfma_f32_16x16x32_f16 v[90:93], v[126:129], v[122:125], v[90:93]
	ds_read_b128 v[122:125], v138 offset:9216
	s_waitcnt lgkmcnt(7)
	v_mfma_f32_16x16x32_f16 v[94:97], v[126:129], v[66:69], v[94:97]
	ds_read_b128 v[66:69], v138 offset:10240
	s_waitcnt lgkmcnt(7)
	v_mfma_f32_16x16x32_f16 v[98:101], v[126:129], v[70:73], v[98:101]
	ds_read_b128 v[70:73], v138 offset:11264
	s_waitcnt lgkmcnt(7)
	v_mfma_f32_16x16x32_f16 v[102:105], v[126:129], v[74:77], v[102:105]
	ds_read_b128 v[74:77], v138 offset:12288
	s_waitcnt lgkmcnt(7)
	v_mfma_f32_16x16x32_f16 v[106:109], v[126:129], v[78:81], v[106:109]
	ds_read_b128 v[78:81], v138 offset:13312
	s_waitcnt lgkmcnt(7)
	v_mfma_f32_16x16x32_f16 v[110:113], v[126:129], v[114:117], v[110:113]
	ds_read_b128 v[114:117], v138 offset:14336
	s_waitcnt lgkmcnt(6)
	v_mfma_f32_16x16x32_f16 v[82:85], v[130:133], v[118:121], v[82:85]
	ds_read_b128 v[118:121], v138 offset:15360
	s_waitcnt lgkmcnt(6)
	v_mfma_f32_16x16x32_f16 v[86:89], v[130:133], v[122:125], v[86:89]
	ds_read_b128 v[126:129], v137 offset:128
	ds_read_b128 v[122:125], v138 offset:16384
	s_waitcnt lgkmcnt(7)
	v_mfma_f32_16x16x32_f16 v[90:93], v[130:133], v[66:69], v[90:93]
	ds_read_b128 v[66:69], v138 offset:17408
	s_waitcnt lgkmcnt(7)
	v_mfma_f32_16x16x32_f16 v[94:97], v[130:133], v[70:73], v[94:97]
	ds_read_b128 v[70:73], v138 offset:18432
	s_waitcnt lgkmcnt(7)
	v_mfma_f32_16x16x32_f16 v[98:101], v[130:133], v[74:77], v[98:101]
	ds_read_b128 v[74:77], v138 offset:19456
	s_waitcnt lgkmcnt(7)
	v_mfma_f32_16x16x32_f16 v[102:105], v[130:133], v[78:81], v[102:105]
	ds_read_b128 v[78:81], v138 offset:20480
	s_waitcnt lgkmcnt(7)
	v_mfma_f32_16x16x32_f16 v[106:109], v[130:133], v[114:117], v[106:109]
	ds_read_b128 v[114:117], v138 offset:21504
	s_waitcnt lgkmcnt(7)
	v_mfma_f32_16x16x32_f16 v[110:113], v[130:133], v[118:121], v[110:113]
	ds_read_b128 v[118:121], v138 offset:22528
	s_waitcnt lgkmcnt(6)
	v_mfma_f32_16x16x32_f16 v[82:85], v[126:129], v[122:125], v[82:85]
	ds_read_b128 v[122:125], v138 offset:23552
	s_waitcnt lgkmcnt(6)
	v_mfma_f32_16x16x32_f16 v[86:89], v[126:129], v[66:69], v[86:89]
	ds_read_b128 v[130:133], v137 offset:192
	ds_read_b128 v[66:69], v138 offset:24576
	s_waitcnt lgkmcnt(7)
	v_mfma_f32_16x16x32_f16 v[90:93], v[126:129], v[70:73], v[90:93]
	ds_read_b128 v[70:73], v138 offset:25600
	s_waitcnt lgkmcnt(7)
	v_mfma_f32_16x16x32_f16 v[94:97], v[126:129], v[74:77], v[94:97]
	ds_read_b128 v[74:77], v138 offset:26624
	s_waitcnt lgkmcnt(7)
	v_mfma_f32_16x16x32_f16 v[98:101], v[126:129], v[78:81], v[98:101]
	ds_read_b128 v[78:81], v138 offset:27648
	s_waitcnt lgkmcnt(7)
	v_mfma_f32_16x16x32_f16 v[102:105], v[126:129], v[114:117], v[102:105]
	ds_read_b128 v[114:117], v138 offset:28672
	s_waitcnt lgkmcnt(7)
	v_mfma_f32_16x16x32_f16 v[106:109], v[126:129], v[118:121], v[106:109]
	ds_read_b128 v[118:121], v138 offset:29696
	s_waitcnt lgkmcnt(7)
	v_mfma_f32_16x16x32_f16 v[110:113], v[126:129], v[122:125], v[110:113]
	ds_read_b128 v[122:125], v138 offset:30720
	s_waitcnt lgkmcnt(6)
	v_mfma_f32_16x16x32_f16 v[82:85], v[130:133], v[66:69], v[82:85]
	ds_read_b128 v[66:69], v138 offset:31744
	s_waitcnt lgkmcnt(6)
	v_mfma_f32_16x16x32_f16 v[86:89], v[130:133], v[70:73], v[86:89]
	s_waitcnt lgkmcnt(5)
	v_mfma_f32_16x16x32_f16 v[90:93], v[130:133], v[74:77], v[90:93]
	s_waitcnt lgkmcnt(4)
	v_mfma_f32_16x16x32_f16 v[94:97], v[130:133], v[78:81], v[94:97]
	s_waitcnt lgkmcnt(3)
	v_mfma_f32_16x16x32_f16 v[98:101], v[130:133], v[114:117], v[98:101]
	s_waitcnt lgkmcnt(2)
	v_mfma_f32_16x16x32_f16 v[102:105], v[130:133], v[118:121], v[102:105]
	s_waitcnt lgkmcnt(1)
	v_mfma_f32_16x16x32_f16 v[106:109], v[130:133], v[122:125], v[106:109]
	s_waitcnt lgkmcnt(0)
	v_mfma_f32_16x16x32_f16 v[110:113], v[130:133], v[66:69], v[110:113]
	v_mov_b32_e32 v66, 0
	v_mov_b32_e32 v67, 0
	v_mov_b32_e32 v68, 0
	v_mov_b32_e32 v69, 0
	v_mov_b32_e32 v70, 0
	v_mov_b32_e32 v71, 0
	v_mov_b32_e32 v72, 0
	v_mov_b32_e32 v73, 0
	v_mov_b32_e32 v74, 0
	v_mov_b32_e32 v75, 0
	v_mov_b32_e32 v76, 0
	v_mov_b32_e32 v77, 0
	v_mov_b32_e32 v78, 0
	v_mov_b32_e32 v79, 0
	v_mov_b32_e32 v80, 0
	v_mov_b32_e32 v81, 0
	s_mov_b32 s66, 1
	s_mov_b32 s65, s37
	s_cmp_eq_u32 s51, 0
	s_cbranch_scc1 .Lfp_is_0
	s_cmp_eq_u32 s51, 1
	s_cbranch_scc1 .Lfp_is_1
	s_cmp_eq_u32 s51, 2
	s_cbranch_scc1 .Lfp_is_2
	s_branch .Lfp_is_3
.Lfp_pe1:
	ds_read_b128 v[126:129], v137
	ds_read_b128 v[114:117], v138 offset:32768
	ds_read_b128 v[118:121], v138 offset:33792
	ds_read_b128 v[122:125], v138 offset:34816
	ds_read_b128 v[66:69], v138 offset:35840
	ds_read_b128 v[70:73], v138 offset:36864
	ds_read_b128 v[74:77], v138 offset:37888
	ds_read_b128 v[78:81], v138 offset:38912
	s_waitcnt lgkmcnt(6)
	v_mfma_f32_16x16x32_f16 v[82:85], v[126:129], v[114:117], v[82:85]
	ds_read_b128 v[114:117], v138 offset:39936
	s_waitcnt lgkmcnt(6)
	v_mfma_f32_16x16x32_f16 v[86:89], v[126:129], v[118:121], v[86:89]
	ds_read_b128 v[130:133], v137 offset:64
	ds_read_b128 v[118:121], v138 offset:40960
	s_waitcnt lgkmcnt(7)
	v_mfma_f32_16x16x32_f16 v[90:93], v[126:129], v[122:125], v[90:93]
	ds_read_b128 v[122:125], v138 offset:41984
	s_waitcnt lgkmcnt(7)
	v_mfma_f32_16x16x32_f16 v[94:97], v[126:129], v[66:69], v[94:97]
	ds_read_b128 v[66:69], v138 offset:43008
	s_waitcnt lgkmcnt(7)
	v_mfma_f32_16x16x32_f16 v[98:101], v[126:129], v[70:73], v[98:101]
	ds_read_b128 v[70:73], v138 offset:44032
	s_waitcnt lgkmcnt(7)
	v_mfma_f32_16x16x32_f16 v[102:105], v[126:129], v[74:77], v[102:105]
	ds_read_b128 v[74:77], v138 offset:45056
	s_waitcnt lgkmcnt(7)
	v_mfma_f32_16x16x32_f16 v[106:109], v[126:129], v[78:81], v[106:109]
	ds_read_b128 v[78:81], v138 offset:46080
	s_waitcnt lgkmcnt(7)
	v_mfma_f32_16x16x32_f16 v[110:113], v[126:129], v[114:117], v[110:113]
	ds_read_b128 v[114:117], v138 offset:47104
	s_waitcnt lgkmcnt(6)
	v_mfma_f32_16x16x32_f16 v[82:85], v[130:133], v[118:121], v[82:85]
	ds_read_b128 v[118:121], v138 offset:48128
	s_waitcnt lgkmcnt(6)
	v_mfma_f32_16x16x32_f16 v[86:89], v[130:133], v[122:125], v[86:89]
	ds_read_b128 v[126:129], v137 offset:128
	ds_read_b128 v[122:125], v138 offset:49152
	s_waitcnt lgkmcnt(7)
	v_mfma_f32_16x16x32_f16 v[90:93], v[130:133], v[66:69], v[90:93]
	ds_read_b128 v[66:69], v138 offset:50176
	s_waitcnt lgkmcnt(7)
	v_mfma_f32_16x16x32_f16 v[94:97], v[130:133], v[70:73], v[94:97]
	ds_read_b128 v[70:73], v138 offset:51200
	s_waitcnt lgkmcnt(7)
	v_mfma_f32_16x16x32_f16 v[98:101], v[130:133], v[74:77], v[98:101]
	ds_read_b128 v[74:77], v138 offset:52224
	s_waitcnt lgkmcnt(7)
	v_mfma_f32_16x16x32_f16 v[102:105], v[130:133], v[78:81], v[102:105]
	ds_read_b128 v[78:81], v138 offset:53248
	s_waitcnt lgkmcnt(7)
	v_mfma_f32_16x16x32_f16 v[106:109], v[130:133], v[114:117], v[106:109]
	ds_read_b128 v[114:117], v138 offset:54272
	s_waitcnt lgkmcnt(7)
	v_mfma_f32_16x16x32_f16 v[110:113], v[130:133], v[118:121], v[110:113]
	ds_read_b128 v[118:121], v138 offset:55296
	s_waitcnt lgkmcnt(6)
	v_mfma_f32_16x16x32_f16 v[82:85], v[126:129], v[122:125], v[82:85]
	ds_read_b128 v[122:125], v138 offset:56320
	s_waitcnt lgkmcnt(6)
	v_mfma_f32_16x16x32_f16 v[86:89], v[126:129], v[66:69], v[86:89]
	ds_read_b128 v[130:133], v137 offset:192
	ds_read_b128 v[66:69], v138 offset:57344
	s_waitcnt lgkmcnt(7)
	v_mfma_f32_16x16x32_f16 v[90:93], v[126:129], v[70:73], v[90:93]
	ds_read_b128 v[70:73], v138 offset:58368
	s_waitcnt lgkmcnt(7)
	v_mfma_f32_16x16x32_f16 v[94:97], v[126:129], v[74:77], v[94:97]
	ds_read_b128 v[74:77], v138 offset:59392
	s_waitcnt lgkmcnt(7)
	v_mfma_f32_16x16x32_f16 v[98:101], v[126:129], v[78:81], v[98:101]
	ds_read_b128 v[78:81], v138 offset:60416
	s_waitcnt lgkmcnt(7)
	v_mfma_f32_16x16x32_f16 v[102:105], v[126:129], v[114:117], v[102:105]
	ds_read_b128 v[114:117], v138 offset:61440
	s_waitcnt lgkmcnt(7)
	v_mfma_f32_16x16x32_f16 v[106:109], v[126:129], v[118:121], v[106:109]
	ds_read_b128 v[118:121], v138 offset:62464
	s_waitcnt lgkmcnt(7)
	v_mfma_f32_16x16x32_f16 v[110:113], v[126:129], v[122:125], v[110:113]
	ds_read_b128 v[122:125], v138 offset:63488
	s_waitcnt lgkmcnt(6)
	v_mfma_f32_16x16x32_f16 v[82:85], v[130:133], v[66:69], v[82:85]
	ds_read_b128 v[66:69], v138 offset:64512
	s_waitcnt lgkmcnt(6)
	v_mfma_f32_16x16x32_f16 v[86:89], v[130:133], v[70:73], v[86:89]
	s_waitcnt lgkmcnt(5)
	v_mfma_f32_16x16x32_f16 v[90:93], v[130:133], v[74:77], v[90:93]
	s_waitcnt lgkmcnt(4)
	v_mfma_f32_16x16x32_f16 v[94:97], v[130:133], v[78:81], v[94:97]
	s_waitcnt lgkmcnt(3)
	v_mfma_f32_16x16x32_f16 v[98:101], v[130:133], v[114:117], v[98:101]
	s_waitcnt lgkmcnt(2)
	v_mfma_f32_16x16x32_f16 v[102:105], v[130:133], v[118:121], v[102:105]
	s_waitcnt lgkmcnt(1)
	v_mfma_f32_16x16x32_f16 v[106:109], v[130:133], v[122:125], v[106:109]
	s_waitcnt lgkmcnt(0)
	v_mfma_f32_16x16x32_f16 v[110:113], v[130:133], v[66:69], v[110:113]
	s_mov_b32 s64, 1
	s_cmp_eq_u32 s51, 0
	s_cbranch_scc1 .Lfp_is_0
	s_cmp_eq_u32 s51, 1
	s_cbranch_scc1 .Lfp_is_1
	s_cmp_eq_u32 s51, 2
	s_cbranch_scc1 .Lfp_is_2
	s_branch .Lfp_is_3
.Lfp_tileend:
	ds_read_b128 v[126:129], v137
	ds_read_b128 v[114:117], v139
	ds_read_b128 v[118:121], v139 offset:1024
	ds_read_b128 v[122:125], v139 offset:2048
	ds_read_b128 v[66:69], v139 offset:3072
	ds_read_b128 v[70:73], v139 offset:4096
	ds_read_b128 v[74:77], v139 offset:5120
	ds_read_b128 v[78:81], v139 offset:6144
	s_waitcnt lgkmcnt(6)
	v_mfma_f32_16x16x32_f16 v[82:85], v[126:129], v[114:117], v[82:85]
	ds_read_b128 v[114:117], v139 offset:7168
	s_waitcnt lgkmcnt(6)
	v_mfma_f32_16x16x32_f16 v[86:89], v[126:129], v[118:121], v[86:89]
	ds_read_b128 v[130:133], v137 offset:64
	ds_read_b128 v[118:121], v139 offset:8192
	s_waitcnt lgkmcnt(7)
	v_mfma_f32_16x16x32_f16 v[90:93], v[126:129], v[122:125], v[90:93]
	ds_read_b128 v[122:125], v139 offset:9216
	s_waitcnt lgkmcnt(7)
	v_mfma_f32_16x16x32_f16 v[94:97], v[126:129], v[66:69], v[94:97]
	ds_read_b128 v[66:69], v139 offset:10240
	s_waitcnt lgkmcnt(7)
	v_mfma_f32_16x16x32_f16 v[98:101], v[126:129], v[70:73], v[98:101]
	ds_read_b128 v[70:73], v139 offset:11264
	s_waitcnt lgkmcnt(7)
	v_mfma_f32_16x16x32_f16 v[102:105], v[126:129], v[74:77], v[102:105]
	ds_read_b128 v[74:77], v139 offset:12288
	s_waitcnt lgkmcnt(7)
	v_mfma_f32_16x16x32_f16 v[106:109], v[126:129], v[78:81], v[106:109]
	ds_read_b128 v[78:81], v139 offset:13312
	s_waitcnt lgkmcnt(7)
	v_mfma_f32_16x16x32_f16 v[110:113], v[126:129], v[114:117], v[110:113]
	ds_read_b128 v[114:117], v139 offset:14336
	s_waitcnt lgkmcnt(6)
	v_mfma_f32_16x16x32_f16 v[82:85], v[130:133], v[118:121], v[82:85]
	ds_read_b128 v[118:121], v139 offset:15360
	s_waitcnt lgkmcnt(6)
	v_mfma_f32_16x16x32_f16 v[86:89], v[130:133], v[122:125], v[86:89]
	ds_read_b128 v[126:129], v137 offset:128
	ds_read_b128 v[122:125], v139 offset:16384
	s_waitcnt lgkmcnt(7)
	v_mfma_f32_16x16x32_f16 v[90:93], v[130:133], v[66:69], v[90:93]
	ds_read_b128 v[66:69], v139 offset:17408
	s_waitcnt lgkmcnt(7)
	v_mfma_f32_16x16x32_f16 v[94:97], v[130:133], v[70:73], v[94:97]
	ds_read_b128 v[70:73], v139 offset:18432
	s_waitcnt lgkmcnt(7)
	v_mfma_f32_16x16x32_f16 v[98:101], v[130:133], v[74:77], v[98:101]
	ds_read_b128 v[74:77], v139 offset:19456
	s_waitcnt lgkmcnt(7)
	v_mfma_f32_16x16x32_f16 v[102:105], v[130:133], v[78:81], v[102:105]
	ds_read_b128 v[78:81], v139 offset:20480
	s_waitcnt lgkmcnt(7)
	v_mfma_f32_16x16x32_f16 v[106:109], v[130:133], v[114:117], v[106:109]
	ds_read_b128 v[114:117], v139 offset:21504
	s_waitcnt lgkmcnt(7)
	v_mfma_f32_16x16x32_f16 v[110:113], v[130:133], v[118:121], v[110:113]
	ds_read_b128 v[118:121], v139 offset:22528
	s_waitcnt lgkmcnt(6)
	v_mfma_f32_16x16x32_f16 v[82:85], v[126:129], v[122:125], v[82:85]
	ds_read_b128 v[122:125], v139 offset:23552
	s_waitcnt lgkmcnt(6)
	v_mfma_f32_16x16x32_f16 v[86:89], v[126:129], v[66:69], v[86:89]
	ds_read_b128 v[130:133], v137 offset:192
	ds_read_b128 v[66:69], v139 offset:24576
	s_waitcnt lgkmcnt(7)
	v_mfma_f32_16x16x32_f16 v[90:93], v[126:129], v[70:73], v[90:93]
	ds_read_b128 v[70:73], v139 offset:25600
	s_waitcnt lgkmcnt(7)
	v_mfma_f32_16x16x32_f16 v[94:97], v[126:129], v[74:77], v[94:97]
	ds_read_b128 v[74:77], v139 offset:26624
	s_waitcnt lgkmcnt(7)
	v_mfma_f32_16x16x32_f16 v[98:101], v[126:129], v[78:81], v[98:101]
	ds_read_b128 v[78:81], v139 offset:27648
	s_waitcnt lgkmcnt(7)
	v_mfma_f32_16x16x32_f16 v[102:105], v[126:129], v[114:117], v[102:105]
	ds_read_b128 v[114:117], v139 offset:28672
	s_waitcnt lgkmcnt(7)
	v_mfma_f32_16x16x32_f16 v[106:109], v[126:129], v[118:121], v[106:109]
	ds_read_b128 v[118:121], v139 offset:29696
	s_waitcnt lgkmcnt(7)
	v_mfma_f32_16x16x32_f16 v[110:113], v[126:129], v[122:125], v[110:113]
	ds_read_b128 v[122:125], v139 offset:30720
	s_waitcnt lgkmcnt(6)
	v_mfma_f32_16x16x32_f16 v[82:85], v[130:133], v[66:69], v[82:85]
	ds_read_b128 v[66:69], v139 offset:31744
	s_waitcnt lgkmcnt(6)
	v_mfma_f32_16x16x32_f16 v[86:89], v[130:133], v[70:73], v[86:89]
	s_waitcnt lgkmcnt(5)
	v_mfma_f32_16x16x32_f16 v[90:93], v[130:133], v[74:77], v[90:93]
	s_waitcnt lgkmcnt(4)
	v_mfma_f32_16x16x32_f16 v[94:97], v[130:133], v[78:81], v[94:97]
	s_waitcnt lgkmcnt(3)
	v_mfma_f32_16x16x32_f16 v[98:101], v[130:133], v[114:117], v[98:101]
	s_waitcnt lgkmcnt(2)
	v_mfma_f32_16x16x32_f16 v[102:105], v[130:133], v[118:121], v[102:105]
	s_waitcnt lgkmcnt(1)
	v_mfma_f32_16x16x32_f16 v[106:109], v[130:133], v[122:125], v[106:109]
	s_waitcnt lgkmcnt(0)
	v_mfma_f32_16x16x32_f16 v[110:113], v[130:133], v[66:69], v[110:113]
	s_nop 7
	s_nop 3
	v_readlane_b32 s62, v166, 0
	v_readlane_b32 s63, v166, 15
	s_cmp_lg_u32 s62, s63
	s_cbranch_scc1 .Lfp_ep_nu
	v_max_f32_e32 v84, v84, v85
	v_max3_f32 v82, v82, v83, v84
	v_ashrrev_i32_e32 v83, 31, v82
	v_or_b32_e32 v83, 0x80000000, v83
	v_xor_b32_e32 v82, v82, v83
	v_max_f32_e32 v88, v88, v89
	v_max3_f32 v86, v86, v87, v88
	v_ashrrev_i32_e32 v87, 31, v86
	v_or_b32_e32 v87, 0x80000000, v87
	v_xor_b32_e32 v86, v86, v87
	v_max_f32_e32 v92, v92, v93
	v_max3_f32 v90, v90, v91, v92
	v_ashrrev_i32_e32 v91, 31, v90
	v_or_b32_e32 v91, 0x80000000, v91
	v_xor_b32_e32 v90, v90, v91
	v_max_f32_e32 v96, v96, v97
	v_max3_f32 v94, v94, v95, v96
	v_ashrrev_i32_e32 v95, 31, v94
	v_or_b32_e32 v95, 0x80000000, v95
	v_xor_b32_e32 v94, v94, v95
	v_max_f32_e32 v100, v100, v101
	v_max3_f32 v98, v98, v99, v100
	v_ashrrev_i32_e32 v99, 31, v98
	v_or_b32_e32 v99, 0x80000000, v99
	v_xor_b32_e32 v98, v98, v99
	v_max_f32_e32 v104, v104, v105
	v_max3_f32 v102, v102, v103, v104
	v_ashrrev_i32_e32 v103, 31, v102
	v_or_b32_e32 v103, 0x80000000, v103
	v_xor_b32_e32 v102, v102, v103
	v_max_f32_e32 v108, v108, v109
	v_max3_f32 v106, v106, v107, v108
	v_ashrrev_i32_e32 v107, 31, v106
	v_or_b32_e32 v107, 0x80000000, v107
	v_xor_b32_e32 v106, v106, v107
	v_max_f32_e32 v112, v112, v113
	v_max3_f32 v110, v110, v111, v112
	v_ashrrev_i32_e32 v111, 31, v110
	v_or_b32_e32 v111, 0x80000000, v111
	v_xor_b32_e32 v110, v110, v111
	s_sub_u32 s52, s62, s60
	s_cmp_lt_u32 s52, 8
	s_cbranch_scc0 .Lfp_ep_glob
	s_lshl_b32 s52, s52, 9
	s_add_u32 s52, s52, 0x24e00
	v_lshl_add_u32 v160, v167, 2, s52
	ds_max_u32 v160, v82
	ds_max_u32 v160, v86 offset:64
	ds_max_u32 v160, v90 offset:128
	ds_max_u32 v160, v94 offset:192
	ds_max_u32 v160, v98 offset:256
	ds_max_u32 v160, v102 offset:320
	ds_max_u32 v160, v106 offset:384
	ds_max_u32 v160, v110 offset:448
	s_branch .Lfp_ep_done

.Lfa_partend:
	ds_write_b128 v136, v[66:69]
	ds_write_b128 v136, v[70:73] offset:64
	ds_write_b128 v136, v[74:77] offset:128
	ds_write_b128 v136, v[78:81] offset:192
	s_cmp_eq_u32 s66, 0
	s_cbranch_scc0 .Lfa_pe1
	ds_read_b128 v[126:129], v137
	ds_read_b128 v[114:117], v138
	ds_read_b128 v[118:121], v138 offset:1024
	ds_read_b128 v[122:125], v138 offset:2048
	ds_read_b128 v[66:69], v138 offset:3072
	ds_read_b128 v[70:73], v138 offset:4096
	ds_read_b128 v[74:77], v138 offset:5120
	ds_read_b128 v[78:81], v138 offset:6144
	s_waitcnt lgkmcnt(6)
	v_mfma_f32_16x16x32_f16 v[82:85], v[114:117], v[126:129], v[82:85]
	ds_read_b128 v[114:117], v138 offset:7168
	s_waitcnt lgkmcnt(6)
	v_mfma_f32_16x16x32_f16 v[86:89], v[118:121], v[126:129], v[86:89]
	ds_read_b128 v[130:133], v137 offset:64
	ds_read_b128 v[118:121], v138 offset:8192
	s_waitcnt lgkmcnt(7)
	v_mfma_f32_16x16x32_f16 v[90:93], v[122:125], v[126:129], v[90:93]
	ds_read_b128 v[122:125], v138 offset:9216
	s_waitcnt lgkmcnt(7)
	v_mfma_f32_16x16x32_f16 v[94:97], v[66:69], v[126:129], v[94:97]
	ds_read_b128 v[66:69], v138 offset:10240
	s_waitcnt lgkmcnt(7)
	v_mfma_f32_16x16x32_f16 v[98:101], v[70:73], v[126:129], v[98:101]
	ds_read_b128 v[70:73], v138 offset:11264
	s_waitcnt lgkmcnt(7)
	v_mfma_f32_16x16x32_f16 v[102:105], v[74:77], v[126:129], v[102:105]
	ds_read_b128 v[74:77], v138 offset:12288
	s_waitcnt lgkmcnt(7)
	v_mfma_f32_16x16x32_f16 v[106:109], v[78:81], v[126:129], v[106:109]
	ds_read_b128 v[78:81], v138 offset:13312
	s_waitcnt lgkmcnt(7)
	v_mfma_f32_16x16x32_f16 v[110:113], v[114:117], v[126:129], v[110:113]
	ds_read_b128 v[114:117], v138 offset:14336
	s_waitcnt lgkmcnt(6)
	v_mfma_f32_16x16x32_f16 v[82:85], v[118:121], v[130:133], v[82:85]
	ds_read_b128 v[118:121], v138 offset:15360
	s_waitcnt lgkmcnt(6)
	v_mfma_f32_16x16x32_f16 v[86:89], v[122:125], v[130:133], v[86:89]
	ds_read_b128 v[126:129], v137 offset:128
	ds_read_b128 v[122:125], v138 offset:16384
	s_waitcnt lgkmcnt(7)
	v_mfma_f32_16x16x32_f16 v[90:93], v[66:69], v[130:133], v[90:93]
	ds_read_b128 v[66:69], v138 offset:17408
	s_waitcnt lgkmcnt(7)
	v_mfma_f32_16x16x32_f16 v[94:97], v[70:73], v[130:133], v[94:97]
	ds_read_b128 v[70:73], v138 offset:18432
	s_waitcnt lgkmcnt(7)
	v_mfma_f32_16x16x32_f16 v[98:101], v[74:77], v[130:133], v[98:101]
	ds_read_b128 v[74:77], v138 offset:19456
	s_waitcnt lgkmcnt(7)
	v_mfma_f32_16x16x32_f16 v[102:105], v[78:81], v[130:133], v[102:105]
	ds_read_b128 v[78:81], v138 offset:20480
	s_waitcnt lgkmcnt(7)
	v_mfma_f32_16x16x32_f16 v[106:109], v[114:117], v[130:133], v[106:109]
	ds_read_b128 v[114:117], v138 offset:21504
	s_waitcnt lgkmcnt(7)
	v_mfma_f32_16x16x32_f16 v[110:113], v[118:121], v[130:133], v[110:113]
	ds_read_b128 v[118:121], v138 offset:22528
	s_waitcnt lgkmcnt(6)
	v_mfma_f32_16x16x32_f16 v[82:85], v[122:125], v[126:129], v[82:85]
	ds_read_b128 v[122:125], v138 offset:23552
	s_waitcnt lgkmcnt(6)
	v_mfma_f32_16x16x32_f16 v[86:89], v[66:69], v[126:129], v[86:89]
	ds_read_b128 v[130:133], v137 offset:192
	ds_read_b128 v[66:69], v138 offset:24576
	s_waitcnt lgkmcnt(7)
	v_mfma_f32_16x16x32_f16 v[90:93], v[70:73], v[126:129], v[90:93]
	ds_read_b128 v[70:73], v138 offset:25600
	s_waitcnt lgkmcnt(7)
	v_mfma_f32_16x16x32_f16 v[94:97], v[74:77], v[126:129], v[94:97]
	ds_read_b128 v[74:77], v138 offset:26624
	s_waitcnt lgkmcnt(7)
	v_mfma_f32_16x16x32_f16 v[98:101], v[78:81], v[126:129], v[98:101]
	ds_read_b128 v[78:81], v138 offset:27648
	s_waitcnt lgkmcnt(7)
	v_mfma_f32_16x16x32_f16 v[102:105], v[114:117], v[126:129], v[102:105]
	ds_read_b128 v[114:117], v138 offset:28672
	s_waitcnt lgkmcnt(7)
	v_mfma_f32_16x16x32_f16 v[106:109], v[118:121], v[126:129], v[106:109]
	ds_read_b128 v[118:121], v138 offset:29696
	s_waitcnt lgkmcnt(7)
	v_mfma_f32_16x16x32_f16 v[110:113], v[122:125], v[126:129], v[110:113]
	ds_read_b128 v[122:125], v138 offset:30720
	s_waitcnt lgkmcnt(6)
	v_mfma_f32_16x16x32_f16 v[82:85], v[66:69], v[130:133], v[82:85]
	ds_read_b128 v[66:69], v138 offset:31744
	s_waitcnt lgkmcnt(6)
	v_mfma_f32_16x16x32_f16 v[86:89], v[70:73], v[130:133], v[86:89]
	s_waitcnt lgkmcnt(5)
	v_mfma_f32_16x16x32_f16 v[90:93], v[74:77], v[130:133], v[90:93]
	s_waitcnt lgkmcnt(4)
	v_mfma_f32_16x16x32_f16 v[94:97], v[78:81], v[130:133], v[94:97]
	s_waitcnt lgkmcnt(3)
	v_mfma_f32_16x16x32_f16 v[98:101], v[114:117], v[130:133], v[98:101]
	s_waitcnt lgkmcnt(2)
	v_mfma_f32_16x16x32_f16 v[102:105], v[118:121], v[130:133], v[102:105]
	s_waitcnt lgkmcnt(1)
	v_mfma_f32_16x16x32_f16 v[106:109], v[122:125], v[130:133], v[106:109]
	s_waitcnt lgkmcnt(0)
	v_mfma_f32_16x16x32_f16 v[110:113], v[66:69], v[130:133], v[110:113]
	v_mov_b32_e32 v66, 0
	v_mov_b32_e32 v67, 0
	v_mov_b32_e32 v68, 0
	v_mov_b32_e32 v69, 0
	v_mov_b32_e32 v70, 0
	v_mov_b32_e32 v71, 0
	v_mov_b32_e32 v72, 0
	v_mov_b32_e32 v73, 0
	v_mov_b32_e32 v74, 0
	v_mov_b32_e32 v75, 0
	v_mov_b32_e32 v76, 0
	v_mov_b32_e32 v77, 0
	v_mov_b32_e32 v78, 0
	v_mov_b32_e32 v79, 0
	v_mov_b32_e32 v80, 0
	v_mov_b32_e32 v81, 0
	s_mov_b32 s66, 1
	s_mov_b32 s65, s37
	s_cmp_eq_u32 s51, 0
	s_cbranch_scc1 .Lfa_is_0
	s_cmp_eq_u32 s51, 1
	s_cbranch_scc1 .Lfa_is_1
	s_cmp_eq_u32 s51, 2
	s_cbranch_scc1 .Lfa_is_2
	s_branch .Lfa_is_3
.Lfa_pe1:
	ds_read_b128 v[126:129], v137
	ds_read_b128 v[114:117], v138 offset:32768
	ds_read_b128 v[118:121], v138 offset:33792
	ds_read_b128 v[122:125], v138 offset:34816
	ds_read_b128 v[66:69], v138 offset:35840
	ds_read_b128 v[70:73], v138 offset:36864
	ds_read_b128 v[74:77], v138 offset:37888
	ds_read_b128 v[78:81], v138 offset:38912
	s_waitcnt lgkmcnt(6)
	v_mfma_f32_16x16x32_f16 v[82:85], v[114:117], v[126:129], v[82:85]
	ds_read_b128 v[114:117], v138 offset:39936
	s_waitcnt lgkmcnt(6)
	v_mfma_f32_16x16x32_f16 v[86:89], v[118:121], v[126:129], v[86:89]
	ds_read_b128 v[130:133], v137 offset:64
	ds_read_b128 v[118:121], v138 offset:40960
	s_waitcnt lgkmcnt(7)
	v_mfma_f32_16x16x32_f16 v[90:93], v[122:125], v[126:129], v[90:93]
	ds_read_b128 v[122:125], v138 offset:41984
	s_waitcnt lgkmcnt(7)
	v_mfma_f32_16x16x32_f16 v[94:97], v[66:69], v[126:129], v[94:97]
	ds_read_b128 v[66:69], v138 offset:43008
	s_waitcnt lgkmcnt(7)
	v_mfma_f32_16x16x32_f16 v[98:101], v[70:73], v[126:129], v[98:101]
	ds_read_b128 v[70:73], v138 offset:44032
	s_waitcnt lgkmcnt(7)
	v_mfma_f32_16x16x32_f16 v[102:105], v[74:77], v[126:129], v[102:105]
	ds_read_b128 v[74:77], v138 offset:45056
	s_waitcnt lgkmcnt(7)
	v_mfma_f32_16x16x32_f16 v[106:109], v[78:81], v[126:129], v[106:109]
	ds_read_b128 v[78:81], v138 offset:46080
	s_waitcnt lgkmcnt(7)
	v_mfma_f32_16x16x32_f16 v[110:113], v[114:117], v[126:129], v[110:113]
	ds_read_b128 v[114:117], v138 offset:47104
	s_waitcnt lgkmcnt(6)
	v_mfma_f32_16x16x32_f16 v[82:85], v[118:121], v[130:133], v[82:85]
	ds_read_b128 v[118:121], v138 offset:48128
	s_waitcnt lgkmcnt(6)
	v_mfma_f32_16x16x32_f16 v[86:89], v[122:125], v[130:133], v[86:89]
	ds_read_b128 v[126:129], v137 offset:128
	ds_read_b128 v[122:125], v138 offset:49152
	s_waitcnt lgkmcnt(7)
	v_mfma_f32_16x16x32_f16 v[90:93], v[66:69], v[130:133], v[90:93]
	ds_read_b128 v[66:69], v138 offset:50176
	s_waitcnt lgkmcnt(7)
	v_mfma_f32_16x16x32_f16 v[94:97], v[70:73], v[130:133], v[94:97]
	ds_read_b128 v[70:73], v138 offset:51200
	s_waitcnt lgkmcnt(7)
	v_mfma_f32_16x16x32_f16 v[98:101], v[74:77], v[130:133], v[98:101]
	ds_read_b128 v[74:77], v138 offset:52224
	s_waitcnt lgkmcnt(7)
	v_mfma_f32_16x16x32_f16 v[102:105], v[78:81], v[130:133], v[102:105]
	ds_read_b128 v[78:81], v138 offset:53248
	s_waitcnt lgkmcnt(7)
	v_mfma_f32_16x16x32_f16 v[106:109], v[114:117], v[130:133], v[106:109]
	ds_read_b128 v[114:117], v138 offset:54272
	s_waitcnt lgkmcnt(7)
	v_mfma_f32_16x16x32_f16 v[110:113], v[118:121], v[130:133], v[110:113]
	ds_read_b128 v[118:121], v138 offset:55296
	s_waitcnt lgkmcnt(6)
	v_mfma_f32_16x16x32_f16 v[82:85], v[122:125], v[126:129], v[82:85]
	ds_read_b128 v[122:125], v138 offset:56320
	s_waitcnt lgkmcnt(6)
	v_mfma_f32_16x16x32_f16 v[86:89], v[66:69], v[126:129], v[86:89]
	s_waitcnt lgkmcnt(5)
	v_mfma_f32_16x16x32_f16 v[90:93], v[70:73], v[126:129], v[90:93]
	s_waitcnt lgkmcnt(4)
	v_mfma_f32_16x16x32_f16 v[94:97], v[74:77], v[126:129], v[94:97]
	s_waitcnt lgkmcnt(3)
	v_mfma_f32_16x16x32_f16 v[98:101], v[78:81], v[126:129], v[98:101]
	s_waitcnt lgkmcnt(2)
	v_mfma_f32_16x16x32_f16 v[102:105], v[114:117], v[126:129], v[102:105]
	s_waitcnt lgkmcnt(1)
	v_mfma_f32_16x16x32_f16 v[106:109], v[118:121], v[126:129], v[106:109]
	s_waitcnt lgkmcnt(0)
	v_mfma_f32_16x16x32_f16 v[110:113], v[122:125], v[126:129], v[110:113]
	s_mov_b32 s64, 1
	s_cmp_eq_u32 s51, 0
	s_cbranch_scc1 .Lfa_is_0
	s_cmp_eq_u32 s51, 1
	s_cbranch_scc1 .Lfa_is_1
	s_cmp_eq_u32 s51, 2
	s_cbranch_scc1 .Lfa_is_2
	s_branch .Lfa_is_3
.Lfa_tileend:
	ds_read_b128 v[126:129], v137
	ds_read_b128 v[114:117], v138 offset:57344
	ds_read_b128 v[118:121], v138 offset:58368
	ds_read_b128 v[122:125], v138 offset:59392
	ds_read_b128 v[66:69], v138 offset:60416
	ds_read_b128 v[70:73], v138 offset:61440
	ds_read_b128 v[74:77], v138 offset:62464
	ds_read_b128 v[78:81], v138 offset:63488
	s_waitcnt lgkmcnt(6)
	v_mfma_f32_16x16x32_f16 v[82:85], v[114:117], v[126:129], v[82:85]
	ds_read_b128 v[114:117], v138 offset:64512
	s_waitcnt lgkmcnt(6)
	v_mfma_f32_16x16x32_f16 v[86:89], v[118:121], v[126:129], v[86:89]
	ds_read_b128 v[130:133], v137 offset:64
	ds_read_b128 v[118:121], v139
	s_waitcnt lgkmcnt(7)
	v_mfma_f32_16x16x32_f16 v[90:93], v[122:125], v[126:129], v[90:93]
	ds_read_b128 v[122:125], v139 offset:1024
	s_waitcnt lgkmcnt(7)
	v_mfma_f32_16x16x32_f16 v[94:97], v[66:69], v[126:129], v[94:97]
	ds_read_b128 v[66:69], v139 offset:2048
	s_waitcnt lgkmcnt(7)
	v_mfma_f32_16x16x32_f16 v[98:101], v[70:73], v[126:129], v[98:101]
	ds_read_b128 v[70:73], v139 offset:3072
	s_waitcnt lgkmcnt(7)
	v_mfma_f32_16x16x32_f16 v[102:105], v[74:77], v[126:129], v[102:105]
	ds_read_b128 v[74:77], v139 offset:4096
	s_waitcnt lgkmcnt(7)
	v_mfma_f32_16x16x32_f16 v[106:109], v[78:81], v[126:129], v[106:109]
	ds_read_b128 v[78:81], v139 offset:5120
	s_waitcnt lgkmcnt(7)
	v_mfma_f32_16x16x32_f16 v[110:113], v[114:117], v[126:129], v[110:113]
	ds_read_b128 v[114:117], v139 offset:6144
	s_waitcnt lgkmcnt(6)
	v_mfma_f32_16x16x32_f16 v[82:85], v[118:121], v[130:133], v[82:85]
	ds_read_b128 v[118:121], v139 offset:7168
	s_waitcnt lgkmcnt(6)
	v_mfma_f32_16x16x32_f16 v[86:89], v[122:125], v[130:133], v[86:89]
	ds_read_b128 v[126:129], v137 offset:128
	ds_read_b128 v[122:125], v139 offset:8192
	s_waitcnt lgkmcnt(7)
	v_mfma_f32_16x16x32_f16 v[90:93], v[66:69], v[130:133], v[90:93]
	ds_read_b128 v[66:69], v139 offset:9216
	s_waitcnt lgkmcnt(7)
	v_mfma_f32_16x16x32_f16 v[94:97], v[70:73], v[130:133], v[94:97]
	ds_read_b128 v[70:73], v139 offset:10240
	s_waitcnt lgkmcnt(7)
	v_mfma_f32_16x16x32_f16 v[98:101], v[74:77], v[130:133], v[98:101]
	ds_read_b128 v[74:77], v139 offset:11264
	s_waitcnt lgkmcnt(7)
	v_mfma_f32_16x16x32_f16 v[102:105], v[78:81], v[130:133], v[102:105]
	ds_read_b128 v[78:81], v139 offset:12288
	s_waitcnt lgkmcnt(7)
	v_mfma_f32_16x16x32_f16 v[106:109], v[114:117], v[130:133], v[106:109]
	ds_read_b128 v[114:117], v139 offset:13312
	s_waitcnt lgkmcnt(7)
	v_mfma_f32_16x16x32_f16 v[110:113], v[118:121], v[130:133], v[110:113]
	ds_read_b128 v[118:121], v139 offset:14336
	s_waitcnt lgkmcnt(6)
	v_mfma_f32_16x16x32_f16 v[82:85], v[122:125], v[126:129], v[82:85]
	ds_read_b128 v[122:125], v139 offset:15360
	s_waitcnt lgkmcnt(6)
	v_mfma_f32_16x16x32_f16 v[86:89], v[66:69], v[126:129], v[86:89]
	s_waitcnt lgkmcnt(5)
	v_mfma_f32_16x16x32_f16 v[90:93], v[70:73], v[126:129], v[90:93]
	s_waitcnt lgkmcnt(4)
	v_mfma_f32_16x16x32_f16 v[94:97], v[74:77], v[126:129], v[94:97]
	s_waitcnt lgkmcnt(3)
	v_mfma_f32_16x16x32_f16 v[98:101], v[78:81], v[126:129], v[98:101]
	s_waitcnt lgkmcnt(2)
	v_mfma_f32_16x16x32_f16 v[102:105], v[114:117], v[126:129], v[102:105]
	s_waitcnt lgkmcnt(1)
	v_mfma_f32_16x16x32_f16 v[106:109], v[118:121], v[126:129], v[106:109]
	s_waitcnt lgkmcnt(0)
	v_mfma_f32_16x16x32_f16 v[110:113], v[122:125], v[126:129], v[110:113]
	s_nop 7
	s_nop 3
	v_max_f32_e32 v82, 0, v82
	v_max_f32_e32 v83, 0, v83
	v_max_f32_e32 v84, 0, v84
	v_max_f32_e32 v85, 0, v85
	v_cvt_pk_f16_f32 v160, v82, v83
	v_cvt_pk_f16_f32 v161, v84, v85
	ds_write_b64 v140, v[160:161]
	v_max_f32_e32 v86, 0, v86
	v_max_f32_e32 v87, 0, v87
	v_max_f32_e32 v88, 0, v88
	v_max_f32_e32 v89, 0, v89
	v_cvt_pk_f16_f32 v162, v86, v87
	v_cvt_pk_f16_f32 v163, v88, v89
	ds_write_b64 v140, v[162:163] offset:32
	v_max_f32_e32 v90, 0, v90
	v_max_f32_e32 v91, 0, v91
	v_max_f32_e32 v92, 0, v92
	v_max_f32_e32 v93, 0, v93
	v_cvt_pk_f16_f32 v160, v90, v91
	v_cvt_pk_f16_f32 v161, v92, v93
	ds_write_b64 v140, v[160:161] offset:64
	v_max_f32_e32 v94, 0, v94
	v_max_f32_e32 v95, 0, v95
	v_max_f32_e32 v96, 0, v96
	v_max_f32_e32 v97, 0, v97
	v_cvt_pk_f16_f32 v162, v94, v95
	v_cvt_pk_f16_f32 v163, v96, v97
	ds_write_b64 v140, v[162:163] offset:96
	v_max_f32_e32 v98, 0, v98
	v_max_f32_e32 v99, 0, v99
	v_max_f32_e32 v100, 0, v100
	v_max_f32_e32 v101, 0, v101
	v_cvt_pk_f16_f32 v160, v98, v99
	v_cvt_pk_f16_f32 v161, v100, v101
	ds_write_b64 v140, v[160:161] offset:128
	v_max_f32_e32 v102, 0, v102
	v_max_f32_e32 v103, 0, v103
	v_max_f32_e32 v104, 0, v104
	v_max_f32_e32 v105, 0, v105
	v_cvt_pk_f16_f32 v162, v102, v103
	v_cvt_pk_f16_f32 v163, v104, v105
	ds_write_b64 v140, v[162:163] offset:160
	v_max_f32_e32 v106, 0, v106
	v_max_f32_e32 v107, 0, v107
	v_max_f32_e32 v108, 0, v108
	v_max_f32_e32 v109, 0, v109
	v_cvt_pk_f16_f32 v160, v106, v107
	v_cvt_pk_f16_f32 v161, v108, v109
	ds_write_b64 v140, v[160:161] offset:192
	v_max_f32_e32 v110, 0, v110
	v_max_f32_e32 v111, 0, v111
	v_max_f32_e32 v112, 0, v112
	v_max_f32_e32 v113, 0, v113
	v_cvt_pk_f16_f32 v162, v110, v111
	v_cvt_pk_f16_f32 v163, v112, v113
	ds_write_b64 v140, v[162:163] offset:224
	s_lshl_b32 s52, s33, 12
	v_add_u32_e32 v158, s52, v142
	ds_read_b128 v[114:117], v141
	ds_read_b128 v[118:121], v141 offset:1088
	ds_read_b128 v[122:125], v141 offset:2176
	ds_read_b128 v[126:129], v141 offset:3264
	s_waitcnt lgkmcnt(3)
	global_store_dwordx4 v158, v[114:117], s[22:23] sc1
	s_waitcnt lgkmcnt(2)
	global_store_dwordx4 v158, v[118:121], s[22:23] offset:1024 sc1
	s_waitcnt lgkmcnt(1)
	global_store_dwordx4 v158, v[122:125], s[22:23] offset:2048 sc1
	s_waitcnt lgkmcnt(0)
	global_store_dwordx4 v158, v[126:129], s[22:23] offset:3072 sc1
	s_nop 1
	s_mov_b32 s66, 0
	s_branch .Lfa_tilestart

.Lfb_pe1:
	ds_read_b128 v[126:129], v137
	ds_read_b128 v[114:117], v138 offset:32768
	ds_read_b128 v[118:121], v138 offset:33792
	ds_read_b128 v[122:125], v138 offset:34816
	ds_read_b128 v[66:69], v138 offset:35840
	ds_read_b128 v[70:73], v138 offset:36864
	ds_read_b128 v[74:77], v138 offset:37888
	ds_read_b128 v[78:81], v138 offset:38912
	s_waitcnt lgkmcnt(6)
	v_mfma_f32_16x16x32_f16 v[82:85], v[114:117], v[126:129], v[82:85]
	ds_read_b128 v[114:117], v138 offset:39936
	s_waitcnt lgkmcnt(6)
	v_mfma_f32_16x16x32_f16 v[86:89], v[118:121], v[126:129], v[86:89]
	ds_read_b128 v[130:133], v137 offset:64
	ds_read_b128 v[118:121], v138 offset:40960
	s_waitcnt lgkmcnt(7)
	v_mfma_f32_16x16x32_f16 v[90:93], v[122:125], v[126:129], v[90:93]
	ds_read_b128 v[122:125], v138 offset:41984
	s_waitcnt lgkmcnt(7)
	v_mfma_f32_16x16x32_f16 v[94:97], v[66:69], v[126:129], v[94:97]
	ds_read_b128 v[66:69], v138 offset:43008
	s_waitcnt lgkmcnt(7)
	v_mfma_f32_16x16x32_f16 v[98:101], v[70:73], v[126:129], v[98:101]
	ds_read_b128 v[70:73], v138 offset:44032
	s_waitcnt lgkmcnt(7)
	v_mfma_f32_16x16x32_f16 v[102:105], v[74:77], v[126:129], v[102:105]
	ds_read_b128 v[74:77], v138 offset:45056
	s_waitcnt lgkmcnt(7)
	v_mfma_f32_16x16x32_f16 v[106:109], v[78:81], v[126:129], v[106:109]
	ds_read_b128 v[78:81], v138 offset:46080
	s_waitcnt lgkmcnt(7)
	v_mfma_f32_16x16x32_f16 v[110:113], v[114:117], v[126:129], v[110:113]
	ds_read_b128 v[114:117], v138 offset:47104
	s_waitcnt lgkmcnt(6)
	v_mfma_f32_16x16x32_f16 v[82:85], v[118:121], v[130:133], v[82:85]
	ds_read_b128 v[118:121], v138 offset:48128
	s_waitcnt lgkmcnt(6)
	v_mfma_f32_16x16x32_f16 v[86:89], v[122:125], v[130:133], v[86:89]
	ds_read_b128 v[126:129], v137 offset:128
	ds_read_b128 v[122:125], v138 offset:49152
	s_waitcnt lgkmcnt(7)
	v_mfma_f32_16x16x32_f16 v[90:93], v[66:69], v[130:133], v[90:93]
	ds_read_b128 v[66:69], v138 offset:50176
	s_waitcnt lgkmcnt(7)
	v_mfma_f32_16x16x32_f16 v[94:97], v[70:73], v[130:133], v[94:97]
	ds_read_b128 v[70:73], v138 offset:51200
	s_waitcnt lgkmcnt(7)
	v_mfma_f32_16x16x32_f16 v[98:101], v[74:77], v[130:133], v[98:101]
	ds_read_b128 v[74:77], v138 offset:52224
	s_waitcnt lgkmcnt(7)
	v_mfma_f32_16x16x32_f16 v[102:105], v[78:81], v[130:133], v[102:105]
	ds_read_b128 v[78:81], v138 offset:53248
	s_waitcnt lgkmcnt(7)
	v_mfma_f32_16x16x32_f16 v[106:109], v[114:117], v[130:133], v[106:109]
	ds_read_b128 v[114:117], v138 offset:54272
	s_waitcnt lgkmcnt(7)
	v_mfma_f32_16x16x32_f16 v[110:113], v[118:121], v[130:133], v[110:113]
	ds_read_b128 v[118:121], v138 offset:55296
	s_waitcnt lgkmcnt(6)
	v_mfma_f32_16x16x32_f16 v[82:85], v[122:125], v[126:129], v[82:85]
	ds_read_b128 v[122:125], v138 offset:56320
	s_waitcnt lgkmcnt(6)
	v_mfma_f32_16x16x32_f16 v[86:89], v[66:69], v[126:129], v[86:89]
	ds_read_b128 v[130:133], v137 offset:192
	ds_read_b128 v[66:69], v138 offset:57344
	s_waitcnt lgkmcnt(7)
	v_mfma_f32_16x16x32_f16 v[90:93], v[70:73], v[126:129], v[90:93]
	ds_read_b128 v[70:73], v138 offset:58368
	s_waitcnt lgkmcnt(7)
	v_mfma_f32_16x16x32_f16 v[94:97], v[74:77], v[126:129], v[94:97]
	ds_read_b128 v[74:77], v138 offset:59392
	s_waitcnt lgkmcnt(7)
	v_mfma_f32_16x16x32_f16 v[98:101], v[78:81], v[126:129], v[98:101]
	ds_read_b128 v[78:81], v138 offset:60416
	s_waitcnt lgkmcnt(7)
	v_mfma_f32_16x16x32_f16 v[102:105], v[114:117], v[126:129], v[102:105]
	ds_read_b128 v[114:117], v138 offset:61440
	s_waitcnt lgkmcnt(7)
	v_mfma_f32_16x16x32_f16 v[106:109], v[118:121], v[126:129], v[106:109]
	ds_read_b128 v[118:121], v138 offset:62464
	s_waitcnt lgkmcnt(7)
	v_mfma_f32_16x16x32_f16 v[110:113], v[122:125], v[126:129], v[110:113]
	ds_read_b128 v[122:125], v138 offset:63488
	s_waitcnt lgkmcnt(6)
	v_mfma_f32_16x16x32_f16 v[82:85], v[66:69], v[130:133], v[82:85]
	ds_read_b128 v[66:69], v138 offset:64512
	s_waitcnt lgkmcnt(6)
	v_mfma_f32_16x16x32_f16 v[86:89], v[70:73], v[130:133], v[86:89]
	s_waitcnt lgkmcnt(5)
	v_mfma_f32_16x16x32_f16 v[90:93], v[74:77], v[130:133], v[90:93]
	s_waitcnt lgkmcnt(4)
	v_mfma_f32_16x16x32_f16 v[94:97], v[78:81], v[130:133], v[94:97]
	s_waitcnt lgkmcnt(3)
	v_mfma_f32_16x16x32_f16 v[98:101], v[114:117], v[130:133], v[98:101]
	s_waitcnt lgkmcnt(2)
	v_mfma_f32_16x16x32_f16 v[102:105], v[118:121], v[130:133], v[102:105]
	s_waitcnt lgkmcnt(1)
	v_mfma_f32_16x16x32_f16 v[106:109], v[122:125], v[130:133], v[106:109]
	s_waitcnt lgkmcnt(0)
	v_mfma_f32_16x16x32_f16 v[110:113], v[66:69], v[130:133], v[110:113]
	s_mov_b32 s64, 1
	s_cmp_eq_u32 s51, 0
	s_cbranch_scc1 .Lfb_is_0
	s_cmp_eq_u32 s51, 1
	s_cbranch_scc1 .Lfb_is_1
	s_cmp_eq_u32 s51, 2
	s_cbranch_scc1 .Lfb_is_2
	s_branch .Lfb_is_3
.Lfb_tileend:
	ds_read_b128 v[126:129], v137
	ds_read_b128 v[114:117], v139
	ds_read_b128 v[118:121], v139 offset:1024
	ds_read_b128 v[122:125], v139 offset:2048
	ds_read_b128 v[66:69], v139 offset:3072
	ds_read_b128 v[70:73], v139 offset:4096
	ds_read_b128 v[74:77], v139 offset:5120
	ds_read_b128 v[78:81], v139 offset:6144
	s_waitcnt lgkmcnt(6)
	v_mfma_f32_16x16x32_f16 v[82:85], v[114:117], v[126:129], v[82:85]
	ds_read_b128 v[114:117], v139 offset:7168
	s_waitcnt lgkmcnt(6)
	v_mfma_f32_16x16x32_f16 v[86:89], v[118:121], v[126:129], v[86:89]
	ds_read_b128 v[130:133], v137 offset:64
	ds_read_b128 v[118:121], v139 offset:8192
	s_waitcnt lgkmcnt(7)
	v_mfma_f32_16x16x32_f16 v[90:93], v[122:125], v[126:129], v[90:93]
	ds_read_b128 v[122:125], v139 offset:9216
	s_waitcnt lgkmcnt(7)
	v_mfma_f32_16x16x32_f16 v[94:97], v[66:69], v[126:129], v[94:97]
	ds_read_b128 v[66:69], v139 offset:10240
	s_waitcnt lgkmcnt(7)
	v_mfma_f32_16x16x32_f16 v[98:101], v[70:73], v[126:129], v[98:101]
	ds_read_b128 v[70:73], v139 offset:11264
	s_waitcnt lgkmcnt(7)
	v_mfma_f32_16x16x32_f16 v[102:105], v[74:77], v[126:129], v[102:105]
	ds_read_b128 v[74:77], v139 offset:12288
	s_waitcnt lgkmcnt(7)
	v_mfma_f32_16x16x32_f16 v[106:109], v[78:81], v[126:129], v[106:109]
	ds_read_b128 v[78:81], v139 offset:13312
	s_waitcnt lgkmcnt(7)
	v_mfma_f32_16x16x32_f16 v[110:113], v[114:117], v[126:129], v[110:113]
	ds_read_b128 v[114:117], v139 offset:14336
	s_waitcnt lgkmcnt(6)
	v_mfma_f32_16x16x32_f16 v[82:85], v[118:121], v[130:133], v[82:85]
	ds_read_b128 v[118:121], v139 offset:15360
	s_waitcnt lgkmcnt(6)
	v_mfma_f32_16x16x32_f16 v[86:89], v[122:125], v[130:133], v[86:89]
	ds_read_b128 v[126:129], v137 offset:128
	ds_read_b128 v[122:125], v139 offset:16384
	s_waitcnt lgkmcnt(7)
	v_mfma_f32_16x16x32_f16 v[90:93], v[66:69], v[130:133], v[90:93]
	ds_read_b128 v[66:69], v139 offset:17408
	s_waitcnt lgkmcnt(7)
	v_mfma_f32_16x16x32_f16 v[94:97], v[70:73], v[130:133], v[94:97]
	ds_read_b128 v[70:73], v139 offset:18432
	s_waitcnt lgkmcnt(7)
	v_mfma_f32_16x16x32_f16 v[98:101], v[74:77], v[130:133], v[98:101]
	ds_read_b128 v[74:77], v139 offset:19456
	s_waitcnt lgkmcnt(7)
	v_mfma_f32_16x16x32_f16 v[102:105], v[78:81], v[130:133], v[102:105]
	ds_read_b128 v[78:81], v139 offset:20480
	s_waitcnt lgkmcnt(7)
	v_mfma_f32_16x16x32_f16 v[106:109], v[114:117], v[130:133], v[106:109]
	ds_read_b128 v[114:117], v139 offset:21504
	s_waitcnt lgkmcnt(7)
	v_mfma_f32_16x16x32_f16 v[110:113], v[118:121], v[130:133], v[110:113]
	ds_read_b128 v[118:121], v139 offset:22528
	s_waitcnt lgkmcnt(6)
	v_mfma_f32_16x16x32_f16 v[82:85], v[122:125], v[126:129], v[82:85]
	ds_read_b128 v[122:125], v139 offset:23552
	s_waitcnt lgkmcnt(6)
	v_mfma_f32_16x16x32_f16 v[86:89], v[66:69], v[126:129], v[86:89]
	ds_read_b128 v[130:133], v137 offset:192
	ds_read_b128 v[66:69], v139 offset:24576
	s_waitcnt lgkmcnt(7)
	v_mfma_f32_16x16x32_f16 v[90:93], v[70:73], v[126:129], v[90:93]
	ds_read_b128 v[70:73], v139 offset:25600
	s_waitcnt lgkmcnt(7)
	v_mfma_f32_16x16x32_f16 v[94:97], v[74:77], v[126:129], v[94:97]
	ds_read_b128 v[74:77], v139 offset:26624
	s_waitcnt lgkmcnt(7)
	v_mfma_f32_16x16x32_f16 v[98:101], v[78:81], v[126:129], v[98:101]
	ds_read_b128 v[78:81], v139 offset:27648
	s_waitcnt lgkmcnt(7)
	v_mfma_f32_16x16x32_f16 v[102:105], v[114:117], v[126:129], v[102:105]
	ds_read_b128 v[114:117], v139 offset:28672
	s_waitcnt lgkmcnt(7)
	v_mfma_f32_16x16x32_f16 v[106:109], v[118:121], v[126:129], v[106:109]
	ds_read_b128 v[118:121], v139 offset:29696
	s_waitcnt lgkmcnt(7)
	v_mfma_f32_16x16x32_f16 v[110:113], v[122:125], v[126:129], v[110:113]
	ds_read_b128 v[122:125], v139 offset:30720
	s_waitcnt lgkmcnt(6)
	v_mfma_f32_16x16x32_f16 v[82:85], v[66:69], v[130:133], v[82:85]
	ds_read_b128 v[66:69], v139 offset:31744
	s_waitcnt lgkmcnt(6)
	v_mfma_f32_16x16x32_f16 v[86:89], v[70:73], v[130:133], v[86:89]
	s_waitcnt lgkmcnt(5)
	v_mfma_f32_16x16x32_f16 v[90:93], v[74:77], v[130:133], v[90:93]
	s_waitcnt lgkmcnt(4)
	v_mfma_f32_16x16x32_f16 v[94:97], v[78:81], v[130:133], v[94:97]
	s_waitcnt lgkmcnt(3)
	v_mfma_f32_16x16x32_f16 v[98:101], v[114:117], v[130:133], v[98:101]
	s_waitcnt lgkmcnt(2)
	v_mfma_f32_16x16x32_f16 v[102:105], v[118:121], v[130:133], v[102:105]
	s_waitcnt lgkmcnt(1)
	v_mfma_f32_16x16x32_f16 v[106:109], v[122:125], v[130:133], v[106:109]
	s_waitcnt lgkmcnt(0)
	v_mfma_f32_16x16x32_f16 v[110:113], v[66:69], v[130:133], v[110:113]
	s_nop 7
	s_nop 3
	v_max_f32_e32 v82, 0, v82
	v_max_f32_e32 v83, 0, v83
	v_max_f32_e32 v84, 0, v84
	v_max_f32_e32 v85, 0, v85
	v_cvt_pk_f16_f32 v160, v82, v83
	v_cvt_pk_f16_f32 v161, v84, v85
	ds_write_b64 v140, v[160:161]
	v_max_f32_e32 v86, 0, v86
	v_max_f32_e32 v87, 0, v87
	v_max_f32_e32 v88, 0, v88
	v_max_f32_e32 v89, 0, v89
	v_cvt_pk_f16_f32 v162, v86, v87
	v_cvt_pk_f16_f32 v163, v88, v89
	ds_write_b64 v140, v[162:163] offset:32
	v_max_f32_e32 v90, 0, v90
	v_max_f32_e32 v91, 0, v91
	v_max_f32_e32 v92, 0, v92
	v_max_f32_e32 v93, 0, v93
	v_cvt_pk_f16_f32 v160, v90, v91
	v_cvt_pk_f16_f32 v161, v92, v93
	ds_write_b64 v140, v[160:161] offset:64
	v_max_f32_e32 v94, 0, v94
	v_max_f32_e32 v95, 0, v95
	v_max_f32_e32 v96, 0, v96
	v_max_f32_e32 v97, 0, v97
	v_cvt_pk_f16_f32 v162, v94, v95
	v_cvt_pk_f16_f32 v163, v96, v97
	ds_write_b64 v140, v[162:163] offset:96
	v_max_f32_e32 v98, 0, v98
	v_max_f32_e32 v99, 0, v99
	v_max_f32_e32 v100, 0, v100
	v_max_f32_e32 v101, 0, v101
	v_cvt_pk_f16_f32 v160, v98, v99
	v_cvt_pk_f16_f32 v161, v100, v101
	ds_write_b64 v140, v[160:161] offset:128
	v_max_f32_e32 v102, 0, v102
	v_max_f32_e32 v103, 0, v103
	v_max_f32_e32 v104, 0, v104
	v_max_f32_e32 v105, 0, v105
	v_cvt_pk_f16_f32 v162, v102, v103
	v_cvt_pk_f16_f32 v163, v104, v105
	ds_write_b64 v140, v[162:163] offset:160
	v_max_f32_e32 v106, 0, v106
	v_max_f32_e32 v107, 0, v107
	v_max_f32_e32 v108, 0, v108
	v_max_f32_e32 v109, 0, v109
	v_cvt_pk_f16_f32 v160, v106, v107
	v_cvt_pk_f16_f32 v161, v108, v109
	ds_write_b64 v140, v[160:161] offset:192
	v_max_f32_e32 v110, 0, v110
	v_max_f32_e32 v111, 0, v111
	v_max_f32_e32 v112, 0, v112
	v_max_f32_e32 v113, 0, v113
	v_cvt_pk_f16_f32 v162, v110, v111
	v_cvt_pk_f16_f32 v163, v112, v113
	ds_write_b64 v140, v[162:163] offset:224
	s_lshl_b32 s52, s33, 12
	v_add_u32_e32 v158, s52, v142
	ds_read_b128 v[114:117], v141
	ds_read_b128 v[118:121], v141 offset:1088
	ds_read_b128 v[122:125], v141 offset:2176
	ds_read_b128 v[126:129], v141 offset:3264
	s_waitcnt lgkmcnt(3)
	global_store_dwordx4 v158, v[114:117], s[22:23] sc1
	s_waitcnt lgkmcnt(2)
	global_store_dwordx4 v158, v[118:121], s[22:23] offset:1024 sc1
	s_waitcnt lgkmcnt(1)
	global_store_dwordx4 v158, v[122:125], s[22:23] offset:2048 sc1
	s_waitcnt lgkmcnt(0)
	global_store_dwordx4 v158, v[126:129], s[22:23] offset:3072 sc1
	s_nop 1
	s_mov_b32 s66, 0
	s_branch .Lfb_tilestart
